# merge GEMM epilogue gate/scale loads requested one unit ahead; attention vmax load hoisted
# speedup vs baseline: 1.0012x; 1.0012x over previous
.LBB0_400:
	s_mov_b64 s[8:9], -1
	s_and_b64 vcc, exec, s[6:7]
	s_cbranch_vccz .LBB0_393
	s_mov_b64 s[6:7], s[0:1]
	s_load_dwordx2 s[14:15], s[6:7], 0xd0
	s_ashr_i32 s18, s4, 3
	v_mbcnt_lo_u32_b32 v0, -1, 0
	v_mbcnt_hi_u32_b32 v0, -1, v0
	s_ashr_i32 s19, s18, 31
	v_add_u32_e32 v8, s67, v0
	s_lshl_b64 s[16:17], s[18:19], 11
	v_lshlrev_b32_e32 v2, 2, v8
	v_ashrrev_i32_e32 v3, 31, v2
	v_lshl_add_u64 v[4:5], s[16:17], 0, v[2:3]
	s_and_b32 s23, s4, 7
	v_lshlrev_b64 v[4:5], 5, v[4:5]
	s_waitcnt lgkmcnt(0)
	v_lshl_add_u64 v[4:5], s[14:15], 0, v[4:5]
	s_lshl_b32 s52, s23, 2
	v_lshl_add_u64 v[4:5], v[4:5], 0, s[52:53]
	s_mov_b64 s[4:5], 0x100000
	v_lshl_add_u64 v[6:7], v[4:5], 0, s[4:5]
	s_mov_b32 s4, 0x100000
	v_add_co_u32_e32 v4, vcc, s4, v4
	v_and_b32_e32 v9, 64, v234
	s_nop 0
	v_addc_co_u32_e32 v5, vcc, 0, v5, vcc
	global_load_dword v4, v[4:5], off
	s_nop 0
	global_load_dword v0, v[6:7], off offset:32
	global_load_dword v3, v[6:7], off offset:64
	s_nop 0
	global_load_dword v7, v[6:7], off offset:96
	s_lshl_b32 s100, s18, 2
	s_add_u32 s100, s100, s12
	s_addc_u32 s101, s13, 0
	s_add_u32 s100, s100, s14
	s_addc_u32 s101, s101, s15
	v_mov_b32_e32 v241, 0x20000
	global_load_dword v240, v241, s[100:101] sc1
	v_add_u32_e32 v5, -1, v234
	v_cmp_lt_i32_e32 vcc, v5, v9
	v_add_u32_e32 v10, -2, v234
	v_readfirstlane_b32 s5, v8
	v_cndmask_b32_e32 v5, v5, v234, vcc
	v_lshlrev_b32_e32 v11, 2, v5
	v_cmp_lt_i32_e32 vcc, v10, v9
	s_ashr_i32 s4, s5, 6
	s_waitcnt vmcnt(0)
	v_add_f32_e32 v5, v4, v0
	v_add_f32_e32 v6, v3, v5
	v_add_f32_e32 v7, v7, v6
	ds_bpermute_b32 v0, v11, v7
	v_cndmask_b32_e32 v3, v10, v234, vcc
	v_and_b32_e32 v10, 63, v8
	v_cmp_eq_u32_e32 vcc, 0, v10
	v_lshlrev_b32_e32 v3, 2, v3
	s_waitcnt lgkmcnt(0)
	v_add_f32_e32 v0, v7, v0
	v_cndmask_b32_e32 v0, v0, v7, vcc
	ds_bpermute_b32 v3, v3, v0
	v_add_u32_e32 v11, -4, v234
	v_cmp_lt_i32_e32 vcc, v11, v9
	s_waitcnt lgkmcnt(0)
	v_add_f32_e32 v3, v0, v3
	v_cndmask_b32_e32 v11, v11, v234, vcc
	v_cmp_gt_u32_e32 vcc, 2, v10
	v_lshlrev_b32_e32 v11, 2, v11
	s_nop 0
	v_cndmask_b32_e32 v0, v3, v0, vcc
	ds_bpermute_b32 v3, v11, v0
	v_add_u32_e32 v11, -8, v234
	v_cmp_lt_i32_e32 vcc, v11, v9
	s_waitcnt lgkmcnt(0)
	v_add_f32_e32 v3, v0, v3
	v_cndmask_b32_e32 v11, v11, v234, vcc
	v_cmp_gt_u32_e32 vcc, 4, v10
	v_lshlrev_b32_e32 v11, 2, v11
	s_nop 0
	v_cndmask_b32_e32 v0, v3, v0, vcc
	ds_bpermute_b32 v3, v11, v0
	v_add_u32_e32 v11, -16, v234
	v_cmp_lt_i32_e32 vcc, v11, v9
	s_waitcnt lgkmcnt(0)
	v_add_f32_e32 v3, v0, v3
	v_cndmask_b32_e32 v11, v11, v234, vcc
	v_cmp_gt_u32_e32 vcc, 8, v10
	v_lshlrev_b32_e32 v11, 2, v11
	s_nop 0
	v_cndmask_b32_e32 v0, v3, v0, vcc
	ds_bpermute_b32 v3, v11, v0
	v_subrev_u32_e32 v11, 32, v234
	v_cmp_lt_i32_e32 vcc, v11, v9
	s_waitcnt lgkmcnt(0)
	v_add_f32_e32 v3, v0, v3
	v_cndmask_b32_e32 v11, v11, v234, vcc
	v_cmp_gt_u32_e32 vcc, 16, v10
	v_lshlrev_b32_e32 v11, 2, v11
	s_nop 0
	v_cndmask_b32_e32 v0, v3, v0, vcc
	ds_bpermute_b32 v3, v11, v0
	v_cmp_eq_u32_e32 vcc, 63, v10
	s_waitcnt lgkmcnt(0)
	v_add_f32_e32 v11, v0, v3
	s_and_saveexec_b64 s[8:9], vcc
	s_lshl_b32 s10, s4, 2
	s_add_i32 s10, s10, 0
	v_mov_b32_e32 v3, s10
	ds_write_b32 v3, v11 offset:45056
	s_or_b64 exec, exec, s[8:9]
	s_load_dwordx4 s[8:11], s[6:7], 0x20
	s_cmp_lt_i32 s4, 1
	v_mov_b32_e32 v12, 0
	s_waitcnt lgkmcnt(0)
	s_barrier
	s_cbranch_scc1 .LBB0_406
	s_mov_b32 s6, s4
	v_readlane_b32 s7, v254, 60

.LBB0_450:
	ds_bpermute_b32 v0, v226, v251
	s_add_u32 s8, s14, s12
	s_addc_u32 s9, s15, s13
	s_lshl_b64 s[4:5], s[18:19], 2
	s_add_u32 s4, s8, s4
	s_waitcnt lgkmcnt(0)
	v_add_f32_e32 v2, v251, v0
	ds_bpermute_b32 v0, v226, v238
	s_addc_u32 s5, s9, s5
	v_rcp_f32_e32 v2, v2
	v_mov_b32_e32 v177, v1
	s_cmp_eq_u32 s23, 0
	s_waitcnt lgkmcnt(0)
	v_add_f32_e32 v3, v238, v0
	v_mov_b32_e32 v0, v240
	v_max_f32_e32 v0, v0, v0
	v_max_f32_e32 v0, 0x1e3ce508, v0
	v_div_scale_f32 v4, s[4:5], v0, v0, s73
	v_rcp_f32_e32 v5, v4
	s_mov_b64 s[4:5], 0x23c00000
	v_fma_f32 v6, -v4, v5, 1.0
	v_fmac_f32_e32 v5, v6, v5
	v_div_scale_f32 v6, vcc, s73, v0, s73
	v_mul_f32_e32 v7, v6, v5
	v_fma_f32 v8, -v4, v7, v6
	v_fmac_f32_e32 v7, v8, v5
	v_fma_f32 v4, -v4, v7, v6
	v_div_fmas_f32 v4, v4, v5, v7
	v_div_fixup_f32 v4, v4, v0, s73
	v_mul_f32_e32 v7, v2, v4
	v_mul_f32_e32 v9, v65, v7
	v_mul_f32_e32 v10, v66, v7
	v_rcp_f32_e32 v2, v3
	v_mul_f32_e32 v8, v64, v7
	v_mul_f32_e32 v11, v67, v7
	v_rndne_f32_e32 v9, v9
	v_rndne_f32_e32 v10, v10
	v_rndne_f32_e32 v8, v8
	v_cvt_i32_f32_e32 v9, v9
	v_cvt_i32_f32_e32 v10, v10
	v_rndne_f32_e32 v11, v11
	v_cvt_i32_f32_e32 v8, v8
	v_cvt_i32_f32_e32 v11, v11
	v_mul_f32_e32 v6, v2, v4
	v_lshl_add_u64 v[2:3], s[14:15], 0, v[178:179]
	v_lshl_add_u64 v[2:3], v[2:3], 0, s[52:53]
	v_med3_i32 v9, v9, s84, v236
	v_med3_i32 v10, v10, s84, v236
	v_lshl_add_u64 v[4:5], v[2:3], 0, v[176:177]
	v_med3_i32 v8, v8, s84, v236
	v_med3_i32 v11, v11, s84, v236
	v_lshlrev_b32_e32 v9, 8, v9
	v_lshlrev_b32_e32 v10, 16, v10
	v_lshl_add_u64 v[2:3], v[4:5], 0, s[4:5]
	v_and_b32_e32 v9, 0xff00, v9
	v_and_b32_e32 v10, 0xff0000, v10
	v_perm_b32 v8, v11, v8, s60
	s_mov_b32 s4, 0x23c00000
	v_or3_b32 v10, v8, v9, v10
	v_add_co_u32_e32 v8, vcc, s4, v4
	v_mul_f32_e32 v11, v51, v7
	s_nop 0
	v_addc_co_u32_e32 v9, vcc, 0, v5, vcc
	global_store_dword v[8:9], v10, off
	v_mul_f32_e32 v9, v49, v7
	v_mul_f32_e32 v10, v50, v7
	v_mul_f32_e32 v8, v48, v7
	v_rndne_f32_e32 v9, v9
	v_rndne_f32_e32 v10, v10
	v_rndne_f32_e32 v8, v8
	v_cvt_i32_f32_e32 v9, v9
	v_cvt_i32_f32_e32 v10, v10
	v_rndne_f32_e32 v11, v11
	v_cvt_i32_f32_e32 v8, v8
	v_cvt_i32_f32_e32 v11, v11
	v_med3_i32 v9, v9, s84, v236
	v_med3_i32 v10, v10, s84, v236
	v_med3_i32 v8, v8, s84, v236
	v_med3_i32 v11, v11, s84, v236
	v_lshlrev_b32_e32 v9, 8, v9
	v_lshlrev_b32_e32 v10, 16, v10
	v_and_b32_e32 v9, 0xff00, v9
	v_and_b32_e32 v10, 0xff0000, v10
	v_perm_b32 v8, v11, v8, s60
	v_or3_b32 v8, v8, v9, v10
	v_mul_f32_e32 v9, v33, v6
	v_mul_f32_e32 v10, v34, v6
	global_store_dword v[2:3], v8, off offset:32
	v_mul_f32_e32 v8, v32, v6
	v_mul_f32_e32 v11, v35, v6
	v_rndne_f32_e32 v9, v9
	v_rndne_f32_e32 v10, v10
	v_rndne_f32_e32 v8, v8
	v_cvt_i32_f32_e32 v9, v9
	v_cvt_i32_f32_e32 v10, v10
	v_rndne_f32_e32 v11, v11
	v_cvt_i32_f32_e32 v8, v8
	v_cvt_i32_f32_e32 v11, v11
	v_med3_i32 v9, v9, s84, v236
	v_med3_i32 v10, v10, s84, v236
	v_med3_i32 v8, v8, s84, v236
	v_med3_i32 v11, v11, s84, v236
	v_lshlrev_b32_e32 v9, 8, v9
	v_lshlrev_b32_e32 v10, 16, v10
	s_mov_b32 s4, 0x23c04000
	v_and_b32_e32 v9, 0xff00, v9
	v_and_b32_e32 v10, 0xff0000, v10
	v_perm_b32 v8, v11, v8, s60
	v_add_co_u32_e32 v4, vcc, s4, v4
	v_or3_b32 v8, v8, v9, v10
	s_nop 0
	v_addc_co_u32_e32 v5, vcc, 0, v5, vcc
	v_mul_f32_e32 v9, v17, v6
	v_mul_f32_e32 v10, v18, v6
	global_store_dword v[4:5], v8, off
	v_mul_f32_e32 v8, v16, v6
	v_mul_f32_e32 v11, v19, v6
	v_rndne_f32_e32 v9, v9
	v_rndne_f32_e32 v10, v10
	v_rndne_f32_e32 v8, v8
	v_cvt_i32_f32_e32 v9, v9
	v_cvt_i32_f32_e32 v10, v10
	v_rndne_f32_e32 v11, v11
	v_cvt_i32_f32_e32 v8, v8
	v_cvt_i32_f32_e32 v11, v11
	v_med3_i32 v9, v9, s84, v236
	v_med3_i32 v10, v10, s84, v236
	v_med3_i32 v8, v8, s84, v236
	v_med3_i32 v11, v11, s84, v236
	v_lshlrev_b32_e32 v9, 8, v9
	v_lshlrev_b32_e32 v10, 16, v10
	v_and_b32_e32 v9, 0xff00, v9
	v_and_b32_e32 v10, 0xff0000, v10
	v_perm_b32 v8, v11, v8, s60
	v_or3_b32 v8, v8, v9, v10
	v_mul_f32_e32 v9, v69, v7
	v_mul_f32_e32 v10, v70, v7
	global_store_dword v[4:5], v8, off offset:32
	v_mul_f32_e32 v8, v68, v7
	v_mul_f32_e32 v11, v71, v7
	v_rndne_f32_e32 v9, v9
	v_rndne_f32_e32 v10, v10
	v_rndne_f32_e32 v8, v8
	v_cvt_i32_f32_e32 v9, v9
	v_cvt_i32_f32_e32 v10, v10
	v_rndne_f32_e32 v11, v11
	v_cvt_i32_f32_e32 v8, v8
	v_cvt_i32_f32_e32 v11, v11
	v_med3_i32 v9, v9, s84, v236
	v_med3_i32 v10, v10, s84, v236
	v_med3_i32 v8, v8, s84, v236
	v_med3_i32 v11, v11, s84, v236
	v_lshlrev_b32_e32 v9, 8, v9
	v_lshlrev_b32_e32 v10, 16, v10
	v_and_b32_e32 v9, 0xff00, v9
	v_and_b32_e32 v10, 0xff0000, v10
	v_perm_b32 v8, v11, v8, s60
	v_or3_b32 v8, v8, v9, v10
	v_mul_f32_e32 v9, v53, v7
	v_mul_f32_e32 v10, v54, v7
	global_store_dword v[2:3], v8, off offset:8
	v_mul_f32_e32 v8, v52, v7
	v_mul_f32_e32 v11, v55, v7
	v_rndne_f32_e32 v9, v9
	v_rndne_f32_e32 v10, v10
	v_rndne_f32_e32 v8, v8
	v_cvt_i32_f32_e32 v9, v9
	v_cvt_i32_f32_e32 v10, v10
	v_rndne_f32_e32 v11, v11
	v_cvt_i32_f32_e32 v8, v8
	v_cvt_i32_f32_e32 v11, v11
	v_med3_i32 v9, v9, s84, v236
	v_med3_i32 v10, v10, s84, v236
	v_med3_i32 v8, v8, s84, v236
	v_med3_i32 v11, v11, s84, v236
	v_lshlrev_b32_e32 v9, 8, v9
	v_lshlrev_b32_e32 v10, 16, v10
	v_and_b32_e32 v9, 0xff00, v9
	v_and_b32_e32 v10, 0xff0000, v10
	v_perm_b32 v8, v11, v8, s60
	v_or3_b32 v8, v8, v9, v10
	v_mul_f32_e32 v9, v37, v6
	v_mul_f32_e32 v10, v38, v6
	global_store_dword v[2:3], v8, off offset:40
	v_mul_f32_e32 v8, v36, v6
	v_mul_f32_e32 v11, v39, v6
	v_rndne_f32_e32 v9, v9
	v_rndne_f32_e32 v10, v10
	v_rndne_f32_e32 v8, v8
	v_cvt_i32_f32_e32 v9, v9
	v_cvt_i32_f32_e32 v10, v10
	v_rndne_f32_e32 v11, v11
	v_cvt_i32_f32_e32 v8, v8
	v_cvt_i32_f32_e32 v11, v11
	v_med3_i32 v9, v9, s84, v236
	v_med3_i32 v10, v10, s84, v236
	v_med3_i32 v8, v8, s84, v236
	v_med3_i32 v11, v11, s84, v236
	v_lshlrev_b32_e32 v9, 8, v9
	v_lshlrev_b32_e32 v10, 16, v10
	v_and_b32_e32 v9, 0xff00, v9
	v_and_b32_e32 v10, 0xff0000, v10
	v_perm_b32 v8, v11, v8, s60
	v_or3_b32 v8, v8, v9, v10
	v_mul_f32_e32 v9, v21, v6
	v_mul_f32_e32 v10, v22, v6
	global_store_dword v[4:5], v8, off offset:8
	v_mul_f32_e32 v8, v20, v6
	v_mul_f32_e32 v11, v23, v6
	v_rndne_f32_e32 v9, v9
	v_rndne_f32_e32 v10, v10
	v_rndne_f32_e32 v8, v8
	v_cvt_i32_f32_e32 v9, v9
	v_cvt_i32_f32_e32 v10, v10
	v_rndne_f32_e32 v11, v11
	v_cvt_i32_f32_e32 v8, v8
	v_cvt_i32_f32_e32 v11, v11
	v_med3_i32 v9, v9, s84, v236
	v_med3_i32 v10, v10, s84, v236
	v_med3_i32 v8, v8, s84, v236
	v_med3_i32 v11, v11, s84, v236
	v_lshlrev_b32_e32 v9, 8, v9
	v_lshlrev_b32_e32 v10, 16, v10
	v_and_b32_e32 v9, 0xff00, v9
	v_and_b32_e32 v10, 0xff0000, v10
	v_perm_b32 v8, v11, v8, s60
	v_or3_b32 v8, v8, v9, v10
	v_mul_f32_e32 v9, v73, v7
	v_mul_f32_e32 v10, v74, v7
	global_store_dword v[4:5], v8, off offset:40
	v_mul_f32_e32 v8, v72, v7
	v_mul_f32_e32 v11, v75, v7
	v_rndne_f32_e32 v9, v9
	v_rndne_f32_e32 v10, v10
	v_rndne_f32_e32 v8, v8
	v_cvt_i32_f32_e32 v9, v9
	v_cvt_i32_f32_e32 v10, v10
	v_rndne_f32_e32 v11, v11
	v_cvt_i32_f32_e32 v8, v8
	v_cvt_i32_f32_e32 v11, v11
	v_med3_i32 v9, v9, s84, v236
	v_med3_i32 v10, v10, s84, v236
	v_med3_i32 v8, v8, s84, v236
	v_med3_i32 v11, v11, s84, v236
	v_lshlrev_b32_e32 v9, 8, v9
	v_lshlrev_b32_e32 v10, 16, v10
	v_and_b32_e32 v9, 0xff00, v9
	v_and_b32_e32 v10, 0xff0000, v10
	v_perm_b32 v8, v11, v8, s60
	v_or3_b32 v8, v8, v9, v10
	v_mul_f32_e32 v9, v57, v7
	v_mul_f32_e32 v10, v58, v7
	global_store_dword v[2:3], v8, off offset:16
	v_mul_f32_e32 v8, v56, v7
	v_mul_f32_e32 v11, v59, v7
	v_rndne_f32_e32 v9, v9
	v_rndne_f32_e32 v10, v10
	v_rndne_f32_e32 v8, v8
	v_cvt_i32_f32_e32 v9, v9
	v_cvt_i32_f32_e32 v10, v10
	v_rndne_f32_e32 v11, v11
	v_cvt_i32_f32_e32 v8, v8
	v_cvt_i32_f32_e32 v11, v11
	v_med3_i32 v9, v9, s84, v236
	v_med3_i32 v10, v10, s84, v236
	v_med3_i32 v8, v8, s84, v236
	v_med3_i32 v11, v11, s84, v236
	v_lshlrev_b32_e32 v9, 8, v9
	v_lshlrev_b32_e32 v10, 16, v10
	v_and_b32_e32 v9, 0xff00, v9
	v_and_b32_e32 v10, 0xff0000, v10
	v_perm_b32 v8, v11, v8, s60
	v_or3_b32 v8, v8, v9, v10
	v_mul_f32_e32 v9, v41, v6
	v_mul_f32_e32 v10, v42, v6
	global_store_dword v[2:3], v8, off offset:48
	v_mul_f32_e32 v8, v40, v6
	v_mul_f32_e32 v11, v43, v6
	v_rndne_f32_e32 v9, v9
	v_rndne_f32_e32 v10, v10
	v_rndne_f32_e32 v8, v8
	v_cvt_i32_f32_e32 v9, v9
	v_cvt_i32_f32_e32 v10, v10
	v_rndne_f32_e32 v11, v11
	v_cvt_i32_f32_e32 v8, v8
	v_cvt_i32_f32_e32 v11, v11
	v_med3_i32 v9, v9, s84, v236
	v_med3_i32 v10, v10, s84, v236
	v_med3_i32 v8, v8, s84, v236
	v_med3_i32 v11, v11, s84, v236
	v_lshlrev_b32_e32 v9, 8, v9
	v_lshlrev_b32_e32 v10, 16, v10
	v_and_b32_e32 v9, 0xff00, v9
	v_and_b32_e32 v10, 0xff0000, v10
	v_perm_b32 v8, v11, v8, s60
	v_or3_b32 v8, v8, v9, v10
	v_mul_f32_e32 v9, v25, v6
	v_mul_f32_e32 v10, v26, v6
	global_store_dword v[4:5], v8, off offset:16
	v_mul_f32_e32 v8, v24, v6
	v_mul_f32_e32 v11, v27, v6
	v_rndne_f32_e32 v9, v9
	v_rndne_f32_e32 v10, v10
	v_rndne_f32_e32 v8, v8
	v_cvt_i32_f32_e32 v9, v9
	v_cvt_i32_f32_e32 v10, v10
	v_rndne_f32_e32 v11, v11
	v_cvt_i32_f32_e32 v8, v8
	v_cvt_i32_f32_e32 v11, v11
	v_med3_i32 v9, v9, s84, v236
	v_med3_i32 v10, v10, s84, v236
	v_med3_i32 v8, v8, s84, v236
	v_med3_i32 v11, v11, s84, v236
	v_lshlrev_b32_e32 v9, 8, v9
	v_lshlrev_b32_e32 v10, 16, v10
	v_and_b32_e32 v9, 0xff00, v9
	v_and_b32_e32 v10, 0xff0000, v10
	v_perm_b32 v8, v11, v8, s60
	v_or3_b32 v8, v8, v9, v10
	v_mul_f32_e32 v9, v77, v7
	v_mul_f32_e32 v10, v78, v7
	global_store_dword v[4:5], v8, off offset:48
	v_mul_f32_e32 v8, v76, v7
	v_mul_f32_e32 v11, v79, v7
	v_rndne_f32_e32 v9, v9
	v_rndne_f32_e32 v10, v10
	v_rndne_f32_e32 v8, v8
	v_cvt_i32_f32_e32 v9, v9
	v_cvt_i32_f32_e32 v10, v10
	v_rndne_f32_e32 v11, v11
	v_cvt_i32_f32_e32 v8, v8
	v_cvt_i32_f32_e32 v11, v11
	v_med3_i32 v9, v9, s84, v236
	v_med3_i32 v10, v10, s84, v236
	v_med3_i32 v8, v8, s84, v236
	v_med3_i32 v11, v11, s84, v236
	v_lshlrev_b32_e32 v9, 8, v9
	v_lshlrev_b32_e32 v10, 16, v10
	v_and_b32_e32 v9, 0xff00, v9
	v_and_b32_e32 v10, 0xff0000, v10
	v_perm_b32 v8, v11, v8, s60
	v_or3_b32 v8, v8, v9, v10
	v_mul_f32_e32 v9, v61, v7
	v_mul_f32_e32 v10, v62, v7
	global_store_dword v[2:3], v8, off offset:24
	v_mul_f32_e32 v8, v60, v7
	v_mul_f32_e32 v7, v63, v7
	v_rndne_f32_e32 v9, v9
	v_rndne_f32_e32 v10, v10
	v_rndne_f32_e32 v8, v8
	v_cvt_i32_f32_e32 v9, v9
	v_cvt_i32_f32_e32 v10, v10
	v_rndne_f32_e32 v7, v7
	v_cvt_i32_f32_e32 v8, v8
	v_cvt_i32_f32_e32 v7, v7
	v_med3_i32 v9, v9, s84, v236
	v_med3_i32 v10, v10, s84, v236
	v_med3_i32 v8, v8, s84, v236
	v_med3_i32 v7, v7, s84, v236
	v_lshlrev_b32_e32 v9, 8, v9
	v_lshlrev_b32_e32 v10, 16, v10
	v_and_b32_e32 v9, 0xff00, v9
	v_and_b32_e32 v10, 0xff0000, v10
	v_perm_b32 v7, v7, v8, s60
	v_or3_b32 v7, v7, v9, v10
	global_store_dword v[2:3], v7, off offset:56
	v_mul_f32_e32 v3, v45, v6
	v_mul_f32_e32 v7, v46, v6
	v_mul_f32_e32 v2, v44, v6
	v_mul_f32_e32 v8, v47, v6
	v_rndne_f32_e32 v3, v3
	v_rndne_f32_e32 v7, v7
	v_rndne_f32_e32 v2, v2
	v_cvt_i32_f32_e32 v3, v3
	v_cvt_i32_f32_e32 v7, v7
	v_rndne_f32_e32 v8, v8
	v_cvt_i32_f32_e32 v2, v2
	v_cvt_i32_f32_e32 v8, v8
	v_med3_i32 v3, v3, s84, v236
	v_med3_i32 v7, v7, s84, v236
	v_med3_i32 v2, v2, s84, v236
	v_med3_i32 v8, v8, s84, v236
	v_lshlrev_b32_e32 v3, 8, v3
	v_lshlrev_b32_e32 v7, 16, v7
	v_and_b32_e32 v3, 0xff00, v3
	v_and_b32_e32 v7, 0xff0000, v7
	v_perm_b32 v2, v8, v2, s60
	v_or3_b32 v2, v2, v3, v7
	v_mul_f32_e32 v3, v29, v6
	v_mul_f32_e32 v7, v30, v6
	global_store_dword v[4:5], v2, off offset:24
	v_mul_f32_e32 v2, v28, v6
	v_mul_f32_e32 v6, v31, v6
	v_rndne_f32_e32 v3, v3
	v_rndne_f32_e32 v7, v7
	v_rndne_f32_e32 v2, v2
	v_cvt_i32_f32_e32 v3, v3
	v_cvt_i32_f32_e32 v7, v7
	v_rndne_f32_e32 v6, v6
	v_cvt_i32_f32_e32 v2, v2
	v_cvt_i32_f32_e32 v6, v6
	v_med3_i32 v3, v3, s84, v236
	v_med3_i32 v7, v7, s84, v236
	v_med3_i32 v2, v2, s84, v236
	v_med3_i32 v6, v6, s84, v236
	v_lshlrev_b32_e32 v3, 8, v3
	v_lshlrev_b32_e32 v7, 16, v7
	v_and_b32_e32 v3, 0xff00, v3
	v_and_b32_e32 v7, 0xff0000, v7
	v_perm_b32 v2, v6, v2, s60
	s_cselect_b64 s[4:5], -1, 0
	v_or3_b32 v2, v2, v3, v7
	s_and_b64 s[4:5], s[4:5], s[6:7]
	global_store_dword v[4:5], v2, off offset:56
	s_and_saveexec_b64 s[6:7], s[4:5]
	s_cbranch_execz .LBB0_392
	s_add_u32 s4, s14, 0x27c00000
	s_addc_u32 s5, s15, 0
	s_lshl_b64 s[8:9], s[16:17], 2
	v_lshl_add_u64 v[2:3], v[174:175], 2, s[4:5]
	s_add_u32 s4, s4, s8
	v_mul_f32_e32 v0, 0x3c010204, v0
	s_addc_u32 s5, s5, s9
	v_lshl_add_u64 v[4:5], v[172:173], 2, s[4:5]
	global_store_dword v[2:3], v0, off
	global_store_dword v[4:5], v0, off offset:128
	s_branch .LBB0_392

.LBB0_782:
	s_add_u32 s36, s6, 0x13c00000
	s_addc_u32 s37, s7, 0
	s_add_u32 s16, s6, 0x2bc00000
	s_addc_u32 s17, s7, 0
	s_add_u32 s38, s6, 0x27c00000
	s_addc_u32 s39, s7, 0
	s_add_i32 m0, s31, 0x18000
	v_lshl_add_u64 v[8:9], v[8:9], 0, s[56:57]
	s_waitcnt vmcnt(2)
	s_barrier
	global_load_lds_dwordx4 v[8:9], off
	v_lshl_add_u64 v[6:7], v[6:7], 0, s[56:57]
	s_add_i32 m0, s31, 0x1a000
	s_add_i32 s40, s31, 0x8000
	global_load_lds_dwordx4 v[6:7], off
	v_lshl_add_u64 v[2:3], v[2:3], 0, s[56:57]
	s_mov_b32 m0, s40
	s_add_i32 s41, s31, 0xa000
	global_load_lds_dwordx4 v[2:3], off
	v_lshl_add_u64 v[2:3], v[4:5], 0, s[56:57]
	s_mov_b32 m0, s41
	s_lshl_b32 s5, s5, 5
	global_load_lds_dwordx4 v[2:3], off
	v_lshrrev_b32_e32 v3, 1, v0
	v_and_b32_e32 v3, 24, v3
	v_and_b32_e32 v2, 15, v0
	v_lshlrev_b32_e32 v4, 1, v3
	v_lshlrev_b32_e32 v0, 2, v0
	v_lshl_or_b32 v136, s8, 6, v2
	v_lshl_or_b32 v2, v2, 6, v4
	s_lshl_b32 s6, s8, 13
	v_and_b32_e32 v0, 32, v0
	s_and_b32 s5, s5, 0x60
	v_bitop3_b32 v4, v2, s6, v0 bitop3:0xde
	s_lshl_b32 s6, s5, 7
	s_waitcnt vmcnt(4)
	v_bitop3_b32 v137, v2, s6, v0 bitop3:0xde
	s_cmpk_lt_u32 s4, 0x100
	v_mov_b32_e32 v2, 0
	s_mov_b32 s44, 1
	s_cselect_b64 s[18:19], -1, 0
	v_or_b32_e32 v138, s5, v3
	v_add_u32_e32 v139, 0, v4
	v_readlane_b32 s63, v253, 11
	v_readlane_b32 s4, v252, 63
	v_mov_b32_e32 v3, v2
	v_mov_b32_e32 v4, v2
	v_mov_b32_e32 v5, v2
	v_mov_b32_e32 v6, v2
	v_mov_b32_e32 v7, v2
	v_mov_b32_e32 v8, v2
	v_mov_b32_e32 v9, v2
	v_mov_b32_e32 v10, v2
	v_mov_b32_e32 v11, v2
	v_mov_b32_e32 v12, v2
	v_mov_b32_e32 v13, v2
	v_mov_b32_e32 v14, v2
	v_mov_b32_e32 v15, v2
	v_mov_b32_e32 v16, v2
	v_mov_b32_e32 v17, v2
	v_mov_b32_e32 v18, v2
	v_mov_b32_e32 v19, v2
	v_mov_b32_e32 v20, v2
	v_mov_b32_e32 v21, v2
	v_mov_b32_e32 v22, v2
	v_mov_b32_e32 v23, v2
	v_mov_b32_e32 v24, v2
	v_mov_b32_e32 v25, v2
	v_mov_b32_e32 v26, v2
	v_mov_b32_e32 v27, v2
	v_mov_b32_e32 v28, v2
	v_mov_b32_e32 v29, v2
	v_mov_b32_e32 v30, v2
	v_mov_b32_e32 v31, v2
	v_mov_b32_e32 v32, v2
	v_mov_b32_e32 v33, v2
	s_barrier
	v_readlane_b32 s5, v253, 0
	s_lshr_b32 s100, s63, 3
	s_lshl_b32 s101, s100, 15
	v_subrev_u32_e32 v178, s101, v136
	v_lshl_add_u32 v178, s4, 8, v178
	v_lshl_add_u32 v186, s4, 8, v136
	s_lshl_b32 s101, s63, 7
	s_and_b32 s101, s101, 0x380
	v_or_b32_e32 v180, s101, v138
	s_lshl_b32 s101, s100, 10
	v_add_u32_e32 v180, s101, v180
	v_mov_b32_e32 v181, 0
	v_mov_b32_e32 v187, 0
	v_lshl_add_u64 v[182:183], s[36:37], 0, v[180:181]
	v_lshl_add_u64 v[186:187], v[186:187], 2, s[38:39]
	v_mov_b32_e32 v184, v178
	v_ashrrev_i32_e32 v185, 31, v184
	v_lshlrev_b64 v[184:185], 12, v[184:185]
	v_lshl_add_u64 v[184:185], v[182:183], 0, v[184:185]
	global_load_dwordx2 v[216:217], v[184:185], off
	global_load_dword v240, v[186:187], off
	v_add_u32_e32 v184, 16, v178
	v_ashrrev_i32_e32 v185, 31, v184
	v_lshlrev_b64 v[184:185], 12, v[184:185]
	v_lshl_add_u64 v[184:185], v[182:183], 0, v[184:185]
	global_load_dwordx2 v[218:219], v[184:185], off
	global_load_dword v241, v[186:187], off offset:64
	v_add_u32_e32 v184, 32, v178
	v_ashrrev_i32_e32 v185, 31, v184
	v_lshlrev_b64 v[184:185], 12, v[184:185]
	v_lshl_add_u64 v[184:185], v[182:183], 0, v[184:185]
	global_load_dwordx2 v[220:221], v[184:185], off
	global_load_dword v242, v[186:187], off offset:128
	v_add_u32_e32 v184, 48, v178
	v_ashrrev_i32_e32 v185, 31, v184
	v_lshlrev_b64 v[184:185], 12, v[184:185]
	v_lshl_add_u64 v[184:185], v[182:183], 0, v[184:185]
	global_load_dwordx2 v[222:223], v[184:185], off
	global_load_dword v243, v[186:187], off offset:192
	v_add_u32_e32 v184, 128, v178
	v_ashrrev_i32_e32 v185, 31, v184
	v_lshlrev_b64 v[184:185], 12, v[184:185]
	v_lshl_add_u64 v[184:185], v[182:183], 0, v[184:185]
	global_load_dwordx2 v[224:225], v[184:185], off
	global_load_dword v244, v[186:187], off offset:512
	v_add_u32_e32 v184, 144, v178
	v_ashrrev_i32_e32 v185, 31, v184
	v_lshlrev_b64 v[184:185], 12, v[184:185]
	v_lshl_add_u64 v[184:185], v[182:183], 0, v[184:185]
	global_load_dwordx2 v[226:227], v[184:185], off
	global_load_dword v245, v[186:187], off offset:576
	v_add_u32_e32 v184, 160, v178
	v_ashrrev_i32_e32 v185, 31, v184
	v_lshlrev_b64 v[184:185], 12, v[184:185]
	v_lshl_add_u64 v[184:185], v[182:183], 0, v[184:185]
	global_load_dwordx2 v[228:229], v[184:185], off
	global_load_dword v246, v[186:187], off offset:640
	v_add_u32_e32 v184, 176, v178
	v_ashrrev_i32_e32 v185, 31, v184
	v_lshlrev_b64 v[184:185], 12, v[184:185]
	v_lshl_add_u64 v[184:185], v[182:183], 0, v[184:185]
	global_load_dwordx2 v[230:231], v[184:185], off
	global_load_dword v247, v[186:187], off offset:704
	s_branch .LBB0_785

.LBB0_785:
	s_lshr_b32 s6, s44, 2
	s_mul_i32 s6, s6, s46
	s_add_i32 s6, s6, s76
	s_cmpk_lt_i32 s6, 0x400
	s_cselect_b64 s[20:21], -1, 0
	s_and_b32 s7, s44, 3
	s_mov_b64 s[8:9], s[12:13]
	s_mov_b64 s[24:25], s[10:11]
	s_lshl_b32 s11, s7, 3
	s_and_b32 s12, s6, 7
	s_lshl_b32 s7, s7, 7
	s_ashr_i32 s6, s6, 3
	s_mov_b32 s5, s62
	s_mov_b32 s10, s59
	s_or_b32 s59, s12, s11
	s_add_i32 s62, s6, s7
	s_and_b64 s[6:7], s[20:21], exec
	s_cselect_b32 s6, s62, s5
	s_cselect_b32 s10, s59, s10
	s_ashr_i32 s7, s6, 31
	s_lshl_b64 s[6:7], s[6:7], 17
	s_add_u32 s12, s26, s6
	s_addc_u32 s13, s27, s7
	s_and_b64 s[6:7], s[20:21], exec
	s_cselect_b32 s7, s13, s9
	s_cselect_b32 s6, s12, s8
	s_ashr_i32 s11, s10, 31
	s_lshl_b64 s[10:11], s[10:11], 16
	s_add_u32 s10, s28, s10
	s_addc_u32 s11, s29, s11
	s_and_b64 s[22:23], s[20:21], exec
	s_cselect_b32 s23, s11, s25
	s_cselect_b32 s22, s10, s24
	s_add_i32 s5, 0, 0x10000
	v_add_u32_e32 v0, s5, v137
	ds_read_b128 v[34:37], v0
	ds_read_b128 v[38:41], v0 offset:1024
	ds_read_b128 v[42:45], v0 offset:2048
	ds_read_b128 v[46:49], v0 offset:3072
	s_add_u32 s50, s8, 0x10080
	s_addc_u32 s51, s9, 0
	s_add_i32 s48, s31, 0xc000
	v_lshl_add_u64 v[82:83], s[50:51], 0, v[104:105]
	s_mov_b32 m0, s48
	ds_read_b128 v[50:53], v139
	ds_read_b128 v[54:57], v139 offset:1024
	ds_read_b128 v[58:61], v139 offset:2048
	ds_read_b128 v[62:65], v139 offset:3072
	ds_read_b128 v[66:69], v139 offset:4096
	ds_read_b128 v[70:73], v139 offset:5120
	ds_read_b128 v[74:77], v139 offset:6144
	ds_read_b128 v[78:81], v139 offset:7168
	global_load_lds_dwordx4 v[82:83], off
	v_lshl_add_u64 v[82:83], s[50:51], 0, v[100:101]
	s_add_i32 s50, s31, 0xe000
	s_mov_b32 m0, s50
	s_nop 0
	global_load_lds_dwordx4 v[82:83], off
	s_waitcnt vmcnt(22)
	s_waitcnt lgkmcnt(0)
	s_barrier
	s_setprio 1
	s_waitcnt lgkmcnt(0)
	v_mfma_i32_16x16x64_i8 v[82:85], v[34:37], v[50:53], 0
	v_mfma_i32_16x16x64_i8 v[50:53], v[42:45], v[50:53], 0
	v_mfma_i32_16x16x64_i8 v[82:85], v[38:41], v[54:57], v[82:85]
	v_mfma_i32_16x16x64_i8 v[50:53], v[46:49], v[54:57], v[50:53]
	v_mfma_i32_16x16x64_i8 v[54:57], v[34:37], v[58:61], 0
	v_mfma_i32_16x16x64_i8 v[58:61], v[42:45], v[58:61], 0
	v_mfma_i32_16x16x64_i8 v[54:57], v[38:41], v[62:65], v[54:57]
	v_mfma_i32_16x16x64_i8 v[58:61], v[46:49], v[62:65], v[58:61]
	v_mfma_i32_16x16x64_i8 v[62:65], v[34:37], v[66:69], 0
	v_mfma_i32_16x16x64_i8 v[66:69], v[42:45], v[66:69], 0
	v_mfma_i32_16x16x64_i8 v[62:65], v[38:41], v[70:73], v[62:65]
	v_mfma_i32_16x16x64_i8 v[66:69], v[46:49], v[70:73], v[66:69]
	v_mfma_i32_16x16x64_i8 v[70:73], v[34:37], v[74:77], 0
	v_mfma_i32_16x16x64_i8 v[74:77], v[42:45], v[74:77], 0
	v_mfma_i32_16x16x64_i8 v[70:73], v[38:41], v[78:81], v[70:73]
	v_mfma_i32_16x16x64_i8 v[74:77], v[46:49], v[78:81], v[74:77]
	s_setprio 0
	s_barrier
	v_lshl_add_u64 v[134:135], s[24:25], 0, v[102:103]
	s_add_i32 s5, s5, s30
	v_lshl_add_u64 v[122:123], v[134:135], 0, s[92:93]
	s_mov_b32 m0, s5
	v_lshl_add_u64 v[160:161], s[24:25], 0, v[98:99]
	s_add_i32 s51, s5, 0x2000
	ds_read_b128 v[78:81], v139 offset:16384
	ds_read_b128 v[86:89], v139 offset:17408
	ds_read_b128 v[90:93], v139 offset:18432
	ds_read_b128 v[94:97], v139 offset:19456
	ds_read_b128 v[106:109], v139 offset:20480
	ds_read_b128 v[110:113], v139 offset:21504
	ds_read_b128 v[114:117], v139 offset:22528
	ds_read_b128 v[118:121], v139 offset:23552
	global_load_lds_dwordx4 v[122:123], off
	v_lshl_add_u64 v[122:123], v[160:161], 0, s[92:93]
	s_mov_b32 m0, s51
	v_lshl_add_u64 v[162:163], s[8:9], 0, v[104:105]
	global_load_lds_dwordx4 v[122:123], off
	v_lshl_add_u64 v[122:123], v[162:163], 0, s[92:93]
	s_mov_b32 m0, s31
	v_lshl_add_u64 v[164:165], s[8:9], 0, v[100:101]
	global_load_lds_dwordx4 v[122:123], off
	v_lshl_add_u64 v[122:123], v[164:165], 0, s[92:93]
	s_mov_b32 m0, s33
	s_nop 0
	global_load_lds_dwordx4 v[122:123], off
	s_waitcnt vmcnt(22)
	s_waitcnt lgkmcnt(0)
	s_barrier
	s_setprio 1
	s_waitcnt lgkmcnt(0)
	v_mfma_i32_16x16x64_i8 v[122:125], v[34:37], v[78:81], 0
	v_mfma_i32_16x16x64_i8 v[78:81], v[42:45], v[78:81], 0
	v_mfma_i32_16x16x64_i8 v[122:125], v[38:41], v[86:89], v[122:125]
	v_mfma_i32_16x16x64_i8 v[78:81], v[46:49], v[86:89], v[78:81]
	v_mfma_i32_16x16x64_i8 v[86:89], v[34:37], v[90:93], 0
	v_mfma_i32_16x16x64_i8 v[90:93], v[42:45], v[90:93], 0
	v_mfma_i32_16x16x64_i8 v[86:89], v[38:41], v[94:97], v[86:89]
	v_mfma_i32_16x16x64_i8 v[90:93], v[46:49], v[94:97], v[90:93]
	v_mfma_i32_16x16x64_i8 v[94:97], v[34:37], v[106:109], 0
	v_mfma_i32_16x16x64_i8 v[34:37], v[34:37], v[114:117], 0
	v_mfma_i32_16x16x64_i8 v[94:97], v[38:41], v[110:113], v[94:97]
	v_mfma_i32_16x16x64_i8 v[34:37], v[38:41], v[118:121], v[34:37]
	v_mfma_i32_16x16x64_i8 v[38:41], v[42:45], v[114:117], 0
	v_mfma_i32_16x16x64_i8 v[106:109], v[42:45], v[106:109], 0
	v_mfma_i32_16x16x64_i8 v[38:41], v[46:49], v[118:121], v[38:41]
	v_mfma_i32_16x16x64_i8 v[106:109], v[46:49], v[110:113], v[106:109]
	s_setprio 0
	s_barrier
	s_add_i32 s52, 0, 0x18000
	v_add_u32_e32 v168, s52, v137
	ds_read_b128 v[42:45], v168
	ds_read_b128 v[46:49], v168 offset:1024
	ds_read_b128 v[110:113], v168 offset:2048
	ds_read_b128 v[114:117], v168 offset:3072
	s_add_u32 s24, s8, 0x10100
	s_addc_u32 s25, s9, 0
	s_mov_b32 m0, s34
	v_lshl_add_u64 v[166:167], s[24:25], 0, v[104:105]
	ds_read_b128 v[118:121], v139 offset:32768
	ds_read_b128 v[126:129], v139 offset:33792
	ds_read_b128 v[130:133], v139 offset:34816
	ds_read_b128 v[140:143], v139 offset:35840
	ds_read_b128 v[144:147], v139 offset:36864
	ds_read_b128 v[148:151], v139 offset:37888
	ds_read_b128 v[152:155], v139 offset:38912
	ds_read_b128 v[156:159], v139 offset:39936
	global_load_lds_dwordx4 v[166:167], off
	v_lshl_add_u64 v[166:167], s[24:25], 0, v[100:101]
	s_mov_b32 m0, s35
	s_nop 0
	global_load_lds_dwordx4 v[166:167], off
	s_waitcnt vmcnt(6)
	s_waitcnt lgkmcnt(0)
	s_barrier
	s_setprio 1
	s_waitcnt lgkmcnt(0)
	v_mfma_i32_16x16x64_i8 v[82:85], v[42:45], v[118:121], v[82:85]
	v_mfma_i32_16x16x64_i8 v[50:53], v[110:113], v[118:121], v[50:53]
	v_mfma_i32_16x16x64_i8 v[54:57], v[42:45], v[130:133], v[54:57]
	v_mfma_i32_16x16x64_i8 v[58:61], v[110:113], v[130:133], v[58:61]
	v_mfma_i32_16x16x64_i8 v[62:65], v[42:45], v[144:147], v[62:65]
	v_mfma_i32_16x16x64_i8 v[66:69], v[110:113], v[144:147], v[66:69]
	v_mfma_i32_16x16x64_i8 v[70:73], v[42:45], v[152:155], v[70:73]
	v_mfma_i32_16x16x64_i8 v[74:77], v[110:113], v[152:155], v[74:77]
	v_mfma_i32_16x16x64_i8 v[82:85], v[46:49], v[126:129], v[82:85]
	v_mfma_i32_16x16x64_i8 v[50:53], v[114:117], v[126:129], v[50:53]
	v_mfma_i32_16x16x64_i8 v[54:57], v[46:49], v[140:143], v[54:57]
	v_mfma_i32_16x16x64_i8 v[58:61], v[114:117], v[140:143], v[58:61]
	v_mfma_i32_16x16x64_i8 v[62:65], v[46:49], v[148:151], v[62:65]
	v_mfma_i32_16x16x64_i8 v[66:69], v[114:117], v[148:151], v[66:69]
	v_mfma_i32_16x16x64_i8 v[70:73], v[46:49], v[156:159], v[70:73]
	v_mfma_i32_16x16x64_i8 v[74:77], v[114:117], v[156:159], v[74:77]
	s_setprio 0
	s_barrier
	s_mov_b64 s[54:55], 0x180
	s_add_i32 s24, s52, s30
	v_lshl_add_u64 v[134:135], v[134:135], 0, s[54:55]
	s_mov_b32 m0, s24
	s_add_i32 s25, s24, 0x2000
	ds_read_b128 v[118:121], v139 offset:49152
	ds_read_b128 v[126:129], v139 offset:50176
	ds_read_b128 v[130:133], v139 offset:51200
	ds_read_b128 v[140:143], v139 offset:52224
	ds_read_b128 v[144:147], v139 offset:53248
	ds_read_b128 v[148:151], v139 offset:54272
	ds_read_b128 v[152:155], v139 offset:55296
	ds_read_b128 v[156:159], v139 offset:56320
	global_load_lds_dwordx4 v[134:135], off
	v_lshl_add_u64 v[134:135], v[160:161], 0, s[54:55]
	s_mov_b32 m0, s25
	s_nop 0
	global_load_lds_dwordx4 v[134:135], off
	v_lshl_add_u64 v[134:135], v[162:163], 0, s[54:55]
	s_mov_b32 m0, s40
	s_nop 0
	global_load_lds_dwordx4 v[134:135], off
	v_lshl_add_u64 v[134:135], v[164:165], 0, s[54:55]
	s_mov_b32 m0, s41
	s_nop 0
	global_load_lds_dwordx4 v[134:135], off
	s_waitcnt vmcnt(6)
	s_waitcnt lgkmcnt(0)
	s_barrier
	s_setprio 1
	s_waitcnt lgkmcnt(0)
	v_mfma_i32_16x16x64_i8 v[78:81], v[110:113], v[118:121], v[78:81]
	v_mfma_i32_16x16x64_i8 v[86:89], v[42:45], v[130:133], v[86:89]
	v_mfma_i32_16x16x64_i8 v[90:93], v[110:113], v[130:133], v[90:93]
	v_mfma_i32_16x16x64_i8 v[94:97], v[42:45], v[144:147], v[94:97]
	v_mfma_i32_16x16x64_i8 v[34:37], v[42:45], v[152:155], v[34:37]
	v_mfma_i32_16x16x64_i8 v[38:41], v[110:113], v[152:155], v[38:41]
	v_mfma_i32_16x16x64_i8 v[122:125], v[42:45], v[118:121], v[122:125]
	v_mfma_i32_16x16x64_i8 v[78:81], v[114:117], v[126:129], v[78:81]
	v_mfma_i32_16x16x64_i8 v[86:89], v[46:49], v[140:143], v[86:89]
	v_mfma_i32_16x16x64_i8 v[90:93], v[114:117], v[140:143], v[90:93]
	v_mfma_i32_16x16x64_i8 v[94:97], v[46:49], v[148:151], v[94:97]
	v_mfma_i32_16x16x64_i8 v[106:109], v[110:113], v[144:147], v[106:109]
	v_mfma_i32_16x16x64_i8 v[34:37], v[46:49], v[156:159], v[34:37]
	v_mfma_i32_16x16x64_i8 v[38:41], v[114:117], v[156:159], v[38:41]
	v_mfma_i32_16x16x64_i8 v[122:125], v[46:49], v[126:129], v[122:125]
	v_mfma_i32_16x16x64_i8 v[106:109], v[114:117], v[148:151], v[106:109]
	s_setprio 0
	s_barrier
	ds_read_b128 v[42:45], v0
	ds_read_b128 v[46:49], v0 offset:1024
	ds_read_b128 v[110:113], v0 offset:2048
	ds_read_b128 v[114:117], v0 offset:3072
	s_add_u32 s8, s8, 0x10180
	s_addc_u32 s9, s9, 0
	s_mov_b32 m0, s48
	v_lshl_add_u64 v[134:135], s[8:9], 0, v[104:105]
	ds_read_b128 v[118:121], v139
	ds_read_b128 v[126:129], v139 offset:1024
	ds_read_b128 v[130:133], v139 offset:2048
	ds_read_b128 v[140:143], v139 offset:3072
	ds_read_b128 v[144:147], v139 offset:4096
	ds_read_b128 v[148:151], v139 offset:5120
	ds_read_b128 v[152:155], v139 offset:6144
	ds_read_b128 v[156:159], v139 offset:7168
	global_load_lds_dwordx4 v[134:135], off
	v_lshl_add_u64 v[134:135], s[8:9], 0, v[100:101]
	s_mov_b32 m0, s50
	s_nop 0
	global_load_lds_dwordx4 v[134:135], off
	s_waitcnt vmcnt(6)
	s_waitcnt lgkmcnt(0)
	s_barrier
	s_setprio 1
	s_waitcnt lgkmcnt(0)
	v_mfma_i32_16x16x64_i8 v[82:85], v[42:45], v[118:121], v[82:85]
	v_mfma_i32_16x16x64_i8 v[50:53], v[110:113], v[118:121], v[50:53]
	v_mfma_i32_16x16x64_i8 v[54:57], v[42:45], v[130:133], v[54:57]
	v_mfma_i32_16x16x64_i8 v[58:61], v[110:113], v[130:133], v[58:61]
	v_mfma_i32_16x16x64_i8 v[62:65], v[42:45], v[144:147], v[62:65]
	v_mfma_i32_16x16x64_i8 v[66:69], v[110:113], v[144:147], v[66:69]
	v_mfma_i32_16x16x64_i8 v[70:73], v[42:45], v[152:155], v[70:73]
	v_mfma_i32_16x16x64_i8 v[82:85], v[46:49], v[126:129], v[82:85]
	v_mfma_i32_16x16x64_i8 v[50:53], v[114:117], v[126:129], v[50:53]
	v_mfma_i32_16x16x64_i8 v[54:57], v[46:49], v[140:143], v[54:57]
	v_mfma_i32_16x16x64_i8 v[58:61], v[114:117], v[140:143], v[58:61]
	v_mfma_i32_16x16x64_i8 v[62:65], v[46:49], v[148:151], v[62:65]
	v_mfma_i32_16x16x64_i8 v[66:69], v[114:117], v[148:151], v[66:69]
	v_mfma_i32_16x16x64_i8 v[70:73], v[46:49], v[156:159], v[70:73]
	v_mfma_i32_16x16x64_i8 v[74:77], v[110:113], v[152:155], v[74:77]
	v_mfma_i32_16x16x64_i8 v[118:121], v[114:117], v[156:159], v[74:77]
	s_setprio 0
	s_barrier
	s_mov_b32 m0, s5
	v_lshl_add_u64 v[134:135], s[22:23], 0, v[102:103]
	s_nop 2
	ds_read_b128 v[74:77], v139 offset:16384
	ds_read_b128 v[126:129], v139 offset:17408
	ds_read_b128 v[130:133], v139 offset:18432
	ds_read_b128 v[140:143], v139 offset:19456
	ds_read_b128 v[144:147], v139 offset:20480
	ds_read_b128 v[148:151], v139 offset:21504
	ds_read_b128 v[152:155], v139 offset:22528
	ds_read_b128 v[156:159], v139 offset:23552
	global_load_lds_dwordx4 v[134:135], off
	v_lshl_add_u64 v[172:173], s[22:23], 0, v[98:99]
	s_mov_b32 m0, s51
	v_lshl_add_u64 v[174:175], s[6:7], 0, v[104:105]
	global_load_lds_dwordx4 v[172:173], off
	s_mov_b32 m0, s31
	v_lshl_add_u64 v[176:177], s[6:7], 0, v[100:101]
	global_load_lds_dwordx4 v[174:175], off
	s_mov_b32 m0, s33
	s_nop 0
	global_load_lds_dwordx4 v[176:177], off
	s_waitcnt vmcnt(6)
	s_waitcnt lgkmcnt(0)
	s_barrier
	s_setprio 1
	s_waitcnt lgkmcnt(0)
	v_mfma_i32_16x16x64_i8 v[122:125], v[42:45], v[74:77], v[122:125]
	v_mfma_i32_16x16x64_i8 v[74:77], v[110:113], v[74:77], v[78:81]
	v_mfma_i32_16x16x64_i8 v[122:125], v[46:49], v[126:129], v[122:125]
	v_mfma_i32_16x16x64_i8 v[126:129], v[114:117], v[126:129], v[74:77]
	v_mfma_i32_16x16x64_i8 v[74:77], v[42:45], v[130:133], v[86:89]
	v_mfma_i32_16x16x64_i8 v[160:163], v[46:49], v[140:143], v[74:77]
	v_mfma_i32_16x16x64_i8 v[74:77], v[110:113], v[130:133], v[90:93]
	v_mfma_i32_16x16x64_i8 v[130:133], v[114:117], v[140:143], v[74:77]
	v_mfma_i32_16x16x64_i8 v[74:77], v[42:45], v[144:147], v[94:97]
	v_mfma_i32_16x16x64_i8 v[34:37], v[42:45], v[152:155], v[34:37]
	v_mfma_i32_16x16x64_i8 v[140:143], v[46:49], v[148:151], v[74:77]
	v_mfma_i32_16x16x64_i8 v[74:77], v[110:113], v[144:147], v[106:109]
	v_mfma_i32_16x16x64_i8 v[34:37], v[46:49], v[156:159], v[34:37]
	v_mfma_i32_16x16x64_i8 v[38:41], v[110:113], v[152:155], v[38:41]
	v_mfma_i32_16x16x64_i8 v[106:109], v[114:117], v[148:151], v[74:77]
	v_mfma_i32_16x16x64_i8 v[110:113], v[114:117], v[156:159], v[38:41]
	s_setprio 0
	s_barrier
	s_nop 3
	ds_read_b128 v[38:41], v168
	ds_read_b128 v[114:117], v168 offset:1024
	ds_read_b128 v[144:147], v168 offset:2048
	ds_read_b128 v[148:151], v168 offset:3072
	s_add_u32 s6, s6, 0x10000
	s_addc_u32 s7, s7, 0
	s_mov_b32 m0, s34
	v_lshl_add_u64 v[86:87], s[6:7], 0, v[104:105]
	ds_read_b128 v[42:45], v139 offset:32768
	ds_read_b128 v[46:49], v139 offset:33792
	ds_read_b128 v[74:77], v139 offset:34816
	ds_read_b128 v[78:81], v139 offset:35840
	ds_read_b128 v[152:155], v139 offset:36864
	ds_read_b128 v[156:159], v139 offset:37888
	ds_read_b128 v[164:167], v139 offset:38912
	ds_read_b128 v[168:171], v139 offset:39936
	global_load_lds_dwordx4 v[86:87], off
	v_lshl_add_u64 v[86:87], s[6:7], 0, v[100:101]
	s_mov_b32 m0, s35
	s_nop 0
	global_load_lds_dwordx4 v[86:87], off
	s_waitcnt vmcnt(6)
	s_waitcnt lgkmcnt(0)
	s_barrier
	s_setprio 1
	s_waitcnt lgkmcnt(0)
	v_mfma_i32_16x16x64_i8 v[82:85], v[38:41], v[42:45], v[82:85]
	v_mfma_i32_16x16x64_i8 v[42:45], v[144:147], v[42:45], v[50:53]
	v_mfma_i32_16x16x64_i8 v[90:93], v[148:151], v[46:49], v[42:45]
	v_mfma_i32_16x16x64_i8 v[42:45], v[38:41], v[74:77], v[54:57]
	v_mfma_i32_16x16x64_i8 v[86:89], v[114:117], v[78:81], v[42:45]
	v_mfma_i32_16x16x64_i8 v[42:45], v[144:147], v[74:77], v[58:61]
	v_mfma_i32_16x16x64_i8 v[94:97], v[114:117], v[46:49], v[82:85]
	v_mfma_i32_16x16x64_i8 v[82:85], v[148:151], v[78:81], v[42:45]
	v_mfma_i32_16x16x64_i8 v[42:45], v[38:41], v[152:155], v[62:65]
	v_mfma_i32_16x16x64_i8 v[78:81], v[114:117], v[156:159], v[42:45]
	v_mfma_i32_16x16x64_i8 v[42:45], v[144:147], v[152:155], v[66:69]
	v_mfma_i32_16x16x64_i8 v[74:77], v[148:151], v[156:159], v[42:45]
	v_mfma_i32_16x16x64_i8 v[42:45], v[38:41], v[164:167], v[70:73]
	v_mfma_i32_16x16x64_i8 v[70:73], v[114:117], v[168:171], v[42:45]
	v_mfma_i32_16x16x64_i8 v[42:45], v[144:147], v[164:167], v[118:121]
	v_mfma_i32_16x16x64_i8 v[66:69], v[148:151], v[168:171], v[42:45]
	s_setprio 0
	s_barrier
	s_mov_b32 m0, s24
	v_lshl_add_u64 v[54:55], v[134:135], 0, s[56:57]
	s_nop 2
	ds_read_b128 v[42:45], v139 offset:49152
	ds_read_b128 v[46:49], v139 offset:50176
	ds_read_b128 v[50:53], v139 offset:51200
	ds_read_b128 v[118:121], v139 offset:52224
	ds_read_b128 v[152:155], v139 offset:53248
	ds_read_b128 v[156:159], v139 offset:54272
	ds_read_b128 v[164:167], v139 offset:55296
	ds_read_b128 v[168:171], v139 offset:56320
	global_load_lds_dwordx4 v[54:55], off
	v_lshl_add_u64 v[54:55], v[172:173], 0, s[56:57]
	s_mov_b32 m0, s25
	s_nop 0
	global_load_lds_dwordx4 v[54:55], off
	v_lshl_add_u64 v[54:55], v[174:175], 0, s[56:57]
	s_mov_b32 m0, s40
	s_nop 0
	global_load_lds_dwordx4 v[54:55], off
	v_lshl_add_u64 v[54:55], v[176:177], 0, s[56:57]
	s_mov_b32 m0, s41
	s_nop 0
	global_load_lds_dwordx4 v[54:55], off
	s_waitcnt vmcnt(6)
	s_waitcnt lgkmcnt(0)
	s_barrier
	s_setprio 1
	s_waitcnt lgkmcnt(0)
	v_mfma_i32_16x16x64_i8 v[54:57], v[38:41], v[42:45], v[122:125]
	v_mfma_i32_16x16x64_i8 v[42:45], v[144:147], v[42:45], v[126:129]
	v_mfma_i32_16x16x64_i8 v[58:61], v[148:151], v[46:49], v[42:45]
	v_mfma_i32_16x16x64_i8 v[42:45], v[38:41], v[50:53], v[160:163]
	v_mfma_i32_16x16x64_i8 v[62:65], v[114:117], v[46:49], v[54:57]
	v_mfma_i32_16x16x64_i8 v[54:57], v[114:117], v[118:121], v[42:45]
	v_mfma_i32_16x16x64_i8 v[42:45], v[144:147], v[50:53], v[130:133]
	v_mfma_i32_16x16x64_i8 v[50:53], v[148:151], v[118:121], v[42:45]
	v_mfma_i32_16x16x64_i8 v[42:45], v[38:41], v[152:155], v[140:143]
	v_mfma_i32_16x16x64_i8 v[34:37], v[38:41], v[164:167], v[34:37]
	v_mfma_i32_16x16x64_i8 v[46:49], v[114:117], v[156:159], v[42:45]
	v_mfma_i32_16x16x64_i8 v[42:45], v[144:147], v[152:155], v[106:109]
	v_mfma_i32_16x16x64_i8 v[38:41], v[114:117], v[168:171], v[34:37]
	v_mfma_i32_16x16x64_i8 v[34:37], v[144:147], v[164:167], v[110:113]
	v_mfma_i32_16x16x64_i8 v[42:45], v[148:151], v[156:159], v[42:45]
	v_mfma_i32_16x16x64_i8 v[34:37], v[148:151], v[168:171], v[34:37]
	s_setprio 0
	s_barrier
	s_andn2_b64 vcc, exec, s[18:19]
	s_cbranch_vccnz .LBB0_787
	s_barrier
.LBB0_787:
	s_lshr_b32 s52, s63, 3
	s_lshl_b32 s5, s52, 15
	v_subrev_u32_e32 v0, s5, v136
	v_lshl_add_u32 v134, s4, 8, v0
	s_lshl_b32 s4, s63, 7
	s_and_b32 s4, s4, 0x380
	v_or_b32_e32 v0, s4, v138
	s_lshl_b32 s4, s52, 10
	s_add_u32 s4, s36, s4
	s_addc_u32 s5, s37, 0
	v_lshl_add_u64 v[108:109], s[4:5], 0, v[0:1]
	v_ashrrev_i32_e32 v135, 31, v134
	s_lshl_b64 s[4:5], s[52:53], 17
	s_add_u32 s4, s38, s4
	v_lshlrev_b64 v[106:107], 12, v[134:135]
	s_addc_u32 s5, s39, s5
	v_lshl_add_u64 v[106:107], v[108:109], 0, v[106:107]
	v_lshl_add_u64 v[148:149], v[134:135], 2, s[4:5]
	v_mov_b64_e32 v[150:151], v[216:217]
	s_nop 0
	v_mov_b32_e32 v106, v240
	v_or_b32_e32 v130, 16, v134
	v_ashrrev_i32_e32 v131, 31, v130
	v_or_b32_e32 v126, 32, v134
	v_ashrrev_i32_e32 v127, 31, v126
	v_or_b32_e32 v122, 48, v134
	v_ashrrev_i32_e32 v123, 31, v122
	v_add_u32_e32 v118, 0x80, v134
	v_ashrrev_i32_e32 v119, 31, v118
	v_add_u32_e32 v114, 0x90, v134
	v_ashrrev_i32_e32 v115, 31, v114
	v_add_u32_e32 v110, 0xa0, v134
	v_ashrrev_i32_e32 v111, 31, v110
	v_cvt_f32_i32_e32 v95, v95
	v_cvt_f32_i32_e32 v94, v94
	v_cvt_f32_i32_e32 v97, v97
	v_cvt_f32_i32_e32 v96, v96
	v_cvt_f32_i32_e32 v91, v91
	v_cvt_f32_i32_e32 v90, v90
	v_cvt_f32_i32_e32 v93, v93
	v_cvt_f32_i32_e32 v92, v92
	s_cmp_gt_u32 s63, 7
	s_cselect_b64 s[8:9], -1, 0
	s_cmp_lt_u32 s63, 8

	v_mul_f32_e32 v152, 0x36bae975, v106
	v_lshlrev_b64 v[106:107], 12, v[130:131]
	v_lshl_add_u64 v[106:107], v[108:109], 0, v[106:107]
	v_mov_b64_e32 v[132:133], v[218:219]
	v_mov_b32_e32 v146, v241
	v_lshlrev_b64 v[106:107], 12, v[126:127]
	v_lshl_add_u64 v[106:107], v[108:109], 0, v[106:107]
	v_mov_b64_e32 v[128:129], v[220:221]
	v_mov_b32_e32 v145, v242
	v_lshlrev_b64 v[106:107], 12, v[122:123]
	v_lshl_add_u64 v[106:107], v[108:109], 0, v[106:107]
	v_mov_b64_e32 v[124:125], v[222:223]
	v_mov_b32_e32 v144, v243
	v_lshlrev_b64 v[106:107], 12, v[118:119]
	v_lshl_add_u64 v[106:107], v[108:109], 0, v[106:107]
	v_mov_b64_e32 v[120:121], v[224:225]
	v_mov_b32_e32 v143, v244
	v_lshlrev_b64 v[106:107], 12, v[114:115]
	v_lshl_add_u64 v[106:107], v[108:109], 0, v[106:107]
	v_mov_b64_e32 v[116:117], v[226:227]
	v_mov_b32_e32 v142, v245
	v_lshlrev_b64 v[106:107], 12, v[110:111]
	v_lshl_add_u64 v[106:107], v[108:109], 0, v[106:107]
	v_mov_b64_e32 v[112:113], v[228:229]
	v_mov_b32_e32 v141, v246
	v_add_u32_e32 v106, 0xb0, v134
	v_ashrrev_i32_e32 v107, 31, v106
	v_lshlrev_b64 v[154:155], 12, v[106:107]
	v_lshl_add_u64 v[108:109], v[108:109], 0, v[154:155]
	v_mov_b64_e32 v[108:109], v[230:231]
	s_nop 0
	v_mov_b32_e32 v140, v247
	v_pk_mul_f32 v[96:97], v[152:153], v[96:97] op_sel_hi:[0,1]
	v_pk_mul_f32 v[94:95], v[152:153], v[94:95] op_sel_hi:[0,1]
	v_pk_mul_f32 v[148:149], v[152:153], v[92:93] op_sel_hi:[0,1]
	v_pk_mul_f32 v[152:153], v[152:153], v[90:91] op_sel_hi:[0,1]
	v_cvt_f32_ubyte1_e32 v91, v150
	v_cvt_f32_ubyte0_e32 v90, v150
	v_cvt_f32_ubyte3_e32 v93, v150
	v_cvt_f32_ubyte2_e32 v92, v150
	v_pk_mul_f32 v[90:91], v[94:95], v[90:91]
	v_pk_mul_f32 v[92:93], v[96:97], v[92:93]
	v_cvt_f32_ubyte1_e32 v95, v151
	v_cvt_f32_ubyte0_e32 v94, v151
	v_cvt_f32_ubyte3_e32 v97, v151
	v_cvt_f32_ubyte2_e32 v96, v151
	v_pk_mul_f32 v[94:95], v[152:153], v[94:95]
	v_pk_mul_f32 v[96:97], v[148:149], v[96:97]
	s_cbranch_scc1 .LBB0_789
	v_lshlrev_b32_e32 v148, 16, v30
	v_and_b32_e32 v149, 0xffff0000, v30
	v_lshlrev_b32_e32 v30, 16, v31
	v_and_b32_e32 v31, 0xffff0000, v31
	v_pk_add_f32 v[92:93], v[92:93], v[30:31]
	v_lshlrev_b32_e32 v30, 16, v32
	v_and_b32_e32 v31, 0xffff0000, v32
	v_pk_add_f32 v[94:95], v[94:95], v[30:31]
	v_lshlrev_b32_e32 v30, 16, v33
	v_and_b32_e32 v31, 0xffff0000, v33
	v_pk_add_f32 v[90:91], v[90:91], v[148:149]
	v_pk_add_f32 v[96:97], v[96:97], v[30:31]
.LBB0_789:
	s_cmp_eq_u64 s[20:21], 0
	s_cbranch_scc1 .Lmg_nopf
	s_lshr_b32 s100, s59, 3
	s_lshl_b32 s101, s100, 15
	v_subrev_u32_e32 v178, s101, v136
	v_lshl_add_u32 v178, s62, 8, v178
	v_lshl_add_u32 v186, s62, 8, v136
	s_lshl_b32 s101, s59, 7
	s_and_b32 s101, s101, 0x380
	v_or_b32_e32 v180, s101, v138
	s_lshl_b32 s101, s100, 10
	v_add_u32_e32 v180, s101, v180
	v_mov_b32_e32 v181, 0
	v_mov_b32_e32 v187, 0
	v_lshl_add_u64 v[182:183], s[36:37], 0, v[180:181]
	v_lshl_add_u64 v[186:187], v[186:187], 2, s[38:39]
	v_mov_b32_e32 v184, v178
	v_ashrrev_i32_e32 v185, 31, v184
	v_lshlrev_b64 v[184:185], 12, v[184:185]
	v_lshl_add_u64 v[184:185], v[182:183], 0, v[184:185]
	global_load_dwordx2 v[216:217], v[184:185], off
	global_load_dword v240, v[186:187], off
	v_add_u32_e32 v184, 16, v178
	v_ashrrev_i32_e32 v185, 31, v184
	v_lshlrev_b64 v[184:185], 12, v[184:185]
	v_lshl_add_u64 v[184:185], v[182:183], 0, v[184:185]
	global_load_dwordx2 v[218:219], v[184:185], off
	global_load_dword v241, v[186:187], off offset:64
	v_add_u32_e32 v184, 32, v178
	v_ashrrev_i32_e32 v185, 31, v184
	v_lshlrev_b64 v[184:185], 12, v[184:185]
	v_lshl_add_u64 v[184:185], v[182:183], 0, v[184:185]
	global_load_dwordx2 v[220:221], v[184:185], off
	global_load_dword v242, v[186:187], off offset:128
	v_add_u32_e32 v184, 48, v178
	v_ashrrev_i32_e32 v185, 31, v184
	v_lshlrev_b64 v[184:185], 12, v[184:185]
	v_lshl_add_u64 v[184:185], v[182:183], 0, v[184:185]
	global_load_dwordx2 v[222:223], v[184:185], off
	global_load_dword v243, v[186:187], off offset:192
	v_add_u32_e32 v184, 128, v178
	v_ashrrev_i32_e32 v185, 31, v184
	v_lshlrev_b64 v[184:185], 12, v[184:185]
	v_lshl_add_u64 v[184:185], v[182:183], 0, v[184:185]
	global_load_dwordx2 v[224:225], v[184:185], off
	global_load_dword v244, v[186:187], off offset:512
	v_add_u32_e32 v184, 144, v178
	v_ashrrev_i32_e32 v185, 31, v184
	v_lshlrev_b64 v[184:185], 12, v[184:185]
	v_lshl_add_u64 v[184:185], v[182:183], 0, v[184:185]
	global_load_dwordx2 v[226:227], v[184:185], off
	global_load_dword v245, v[186:187], off offset:576
	v_add_u32_e32 v184, 160, v178
	v_ashrrev_i32_e32 v185, 31, v184
	v_lshlrev_b64 v[184:185], 12, v[184:185]
	v_lshl_add_u64 v[184:185], v[182:183], 0, v[184:185]
	global_load_dwordx2 v[228:229], v[184:185], off
	global_load_dword v246, v[186:187], off offset:640
	v_add_u32_e32 v184, 176, v178
	v_ashrrev_i32_e32 v185, 31, v184
	v_lshlrev_b64 v[184:185], 12, v[184:185]
	v_lshl_add_u64 v[184:185], v[182:183], 0, v[184:185]
	global_load_dwordx2 v[230:231], v[184:185], off
	global_load_dword v247, v[186:187], off offset:704

.LBB0_791:
	v_cvt_f32_i32_e32 v87, v87
	v_cvt_f32_i32_e32 v86, v86
	v_cvt_f32_i32_e32 v89, v89
	v_cvt_f32_i32_e32 v88, v88
	v_cvt_f32_i32_e32 v83, v83
	v_cvt_f32_i32_e32 v85, v85
	v_cvt_f32_i32_e32 v84, v84
	v_cvt_f32_i32_e32 v82, v82

	v_mul_f32_e32 v90, 0x36bae975, v146
	v_pk_mul_f32 v[88:89], v[90:91], v[88:89] op_sel_hi:[0,1]
	v_pk_mul_f32 v[86:87], v[90:91], v[86:87] op_sel_hi:[0,1]
	v_pk_mul_f32 v[92:93], v[90:91], v[84:85] op_sel_hi:[0,1]
	v_pk_mul_f32 v[90:91], v[90:91], v[82:83] op_sel_hi:[0,1]
	v_cvt_f32_ubyte1_e32 v83, v132
	v_cvt_f32_ubyte0_e32 v82, v132
	v_pk_mul_f32 v[82:83], v[86:87], v[82:83]
	v_cvt_f32_ubyte3_e32 v85, v132
	v_cvt_f32_ubyte2_e32 v84, v132
	v_cvt_f32_ubyte1_e32 v87, v133
	v_cvt_f32_ubyte0_e32 v86, v133
	v_pk_mul_f32 v[84:85], v[88:89], v[84:85]
	v_pk_mul_f32 v[86:87], v[90:91], v[86:87]
	v_cvt_f32_ubyte3_e32 v89, v133
	v_cvt_f32_ubyte2_e32 v88, v133
	v_cndmask_b32_e64 v90, 0, 1, s[8:9]
	v_cmp_ne_u32_e64 s[6:7], 1, v90
	s_andn2_b64 vcc, exec, s[8:9]
	v_pk_mul_f32 v[88:89], v[92:93], v[88:89]
	s_cbranch_vccnz .LBB0_793
	v_lshlrev_b32_e32 v90, 16, v26
	v_and_b32_e32 v91, 0xffff0000, v26
	v_lshlrev_b32_e32 v26, 16, v27
	v_and_b32_e32 v27, 0xffff0000, v27
	v_pk_add_f32 v[84:85], v[84:85], v[26:27]
	v_lshlrev_b32_e32 v26, 16, v28
	v_and_b32_e32 v27, 0xffff0000, v28
	v_pk_add_f32 v[86:87], v[86:87], v[26:27]
	v_lshlrev_b32_e32 v26, 16, v29
	v_and_b32_e32 v27, 0xffff0000, v29
	v_pk_add_f32 v[82:83], v[82:83], v[90:91]
	v_pk_add_f32 v[88:89], v[88:89], v[26:27]

.LBB0_795:
	v_cvt_f32_i32_e32 v79, v79
	v_cvt_f32_i32_e32 v78, v78
	v_cvt_f32_i32_e32 v81, v81
	v_cvt_f32_i32_e32 v80, v80
	v_cvt_f32_i32_e32 v75, v75
	v_cvt_f32_i32_e32 v77, v77
	v_cvt_f32_i32_e32 v76, v76
	v_cvt_f32_i32_e32 v74, v74

	v_mul_f32_e32 v82, 0x36bae975, v145
	v_pk_mul_f32 v[80:81], v[82:83], v[80:81] op_sel_hi:[0,1]
	v_pk_mul_f32 v[78:79], v[82:83], v[78:79] op_sel_hi:[0,1]
	v_pk_mul_f32 v[84:85], v[82:83], v[76:77] op_sel_hi:[0,1]
	v_pk_mul_f32 v[82:83], v[82:83], v[74:75] op_sel_hi:[0,1]
	v_cvt_f32_ubyte1_e32 v75, v128
	v_cvt_f32_ubyte0_e32 v74, v128
	v_cvt_f32_ubyte3_e32 v77, v128
	v_cvt_f32_ubyte2_e32 v76, v128
	v_pk_mul_f32 v[74:75], v[78:79], v[74:75]
	v_pk_mul_f32 v[76:77], v[80:81], v[76:77]
	v_cvt_f32_ubyte1_e32 v79, v129
	v_cvt_f32_ubyte0_e32 v78, v129
	v_cvt_f32_ubyte3_e32 v81, v129
	v_cvt_f32_ubyte2_e32 v80, v129
	v_pk_mul_f32 v[78:79], v[82:83], v[78:79]
	s_and_b64 vcc, exec, s[6:7]
	v_pk_mul_f32 v[80:81], v[84:85], v[80:81]
	s_cbranch_vccnz .LBB0_797
	v_lshlrev_b32_e32 v82, 16, v22
	v_and_b32_e32 v83, 0xffff0000, v22
	v_lshlrev_b32_e32 v22, 16, v23
	v_and_b32_e32 v23, 0xffff0000, v23
	v_pk_add_f32 v[76:77], v[76:77], v[22:23]
	v_lshlrev_b32_e32 v22, 16, v24
	v_and_b32_e32 v23, 0xffff0000, v24
	v_pk_add_f32 v[78:79], v[78:79], v[22:23]
	v_lshlrev_b32_e32 v22, 16, v25
	v_and_b32_e32 v23, 0xffff0000, v25
	v_pk_add_f32 v[74:75], v[74:75], v[82:83]
	v_pk_add_f32 v[80:81], v[80:81], v[22:23]

.LBB0_799:
	v_cvt_f32_i32_e32 v71, v71
	v_cvt_f32_i32_e32 v70, v70
	v_cvt_f32_i32_e32 v73, v73
	v_cvt_f32_i32_e32 v72, v72
	v_cvt_f32_i32_e32 v67, v67
	v_cvt_f32_i32_e32 v69, v69
	v_cvt_f32_i32_e32 v68, v68
	v_cvt_f32_i32_e32 v66, v66

	v_mul_f32_e32 v74, 0x36bae975, v144
	v_pk_mul_f32 v[72:73], v[74:75], v[72:73] op_sel_hi:[0,1]
	v_pk_mul_f32 v[70:71], v[74:75], v[70:71] op_sel_hi:[0,1]
	v_pk_mul_f32 v[76:77], v[74:75], v[68:69] op_sel_hi:[0,1]
	v_pk_mul_f32 v[74:75], v[74:75], v[66:67] op_sel_hi:[0,1]
	v_cvt_f32_ubyte1_e32 v67, v124
	v_cvt_f32_ubyte0_e32 v66, v124
	v_cvt_f32_ubyte3_e32 v69, v124
	v_cvt_f32_ubyte2_e32 v68, v124
	v_pk_mul_f32 v[66:67], v[70:71], v[66:67]
	v_pk_mul_f32 v[68:69], v[72:73], v[68:69]
	v_cvt_f32_ubyte1_e32 v71, v125
	v_cvt_f32_ubyte0_e32 v70, v125
	v_cvt_f32_ubyte3_e32 v73, v125
	v_cvt_f32_ubyte2_e32 v72, v125
	v_pk_mul_f32 v[70:71], v[74:75], v[70:71]
	s_and_b64 vcc, exec, s[6:7]
	v_pk_mul_f32 v[72:73], v[76:77], v[72:73]
	s_cbranch_vccnz .LBB0_801
	v_lshlrev_b32_e32 v74, 16, v18
	v_and_b32_e32 v75, 0xffff0000, v18
	v_lshlrev_b32_e32 v18, 16, v19
	v_and_b32_e32 v19, 0xffff0000, v19
	v_pk_add_f32 v[68:69], v[68:69], v[18:19]
	v_lshlrev_b32_e32 v18, 16, v20
	v_and_b32_e32 v19, 0xffff0000, v20
	v_pk_add_f32 v[70:71], v[70:71], v[18:19]
	v_lshlrev_b32_e32 v18, 16, v21
	v_and_b32_e32 v19, 0xffff0000, v21
	v_pk_add_f32 v[66:67], v[66:67], v[74:75]
	v_pk_add_f32 v[72:73], v[72:73], v[18:19]

.LBB0_803:
	v_cvt_f32_i32_e32 v63, v63
	v_cvt_f32_i32_e32 v62, v62
	v_cvt_f32_i32_e32 v65, v65
	v_cvt_f32_i32_e32 v64, v64
	v_cvt_f32_i32_e32 v59, v59
	v_cvt_f32_i32_e32 v61, v61
	v_cvt_f32_i32_e32 v60, v60
	v_cvt_f32_i32_e32 v58, v58

	v_mul_f32_e32 v66, 0x36bae975, v143
	v_pk_mul_f32 v[64:65], v[66:67], v[64:65] op_sel_hi:[0,1]
	v_pk_mul_f32 v[62:63], v[66:67], v[62:63] op_sel_hi:[0,1]
	v_pk_mul_f32 v[68:69], v[66:67], v[60:61] op_sel_hi:[0,1]
	v_pk_mul_f32 v[66:67], v[66:67], v[58:59] op_sel_hi:[0,1]
	v_cvt_f32_ubyte1_e32 v59, v120
	v_cvt_f32_ubyte0_e32 v58, v120
	v_cvt_f32_ubyte3_e32 v61, v120
	v_cvt_f32_ubyte2_e32 v60, v120
	v_pk_mul_f32 v[58:59], v[62:63], v[58:59]
	v_pk_mul_f32 v[60:61], v[64:65], v[60:61]
	v_cvt_f32_ubyte1_e32 v63, v121
	v_cvt_f32_ubyte0_e32 v62, v121
	v_cvt_f32_ubyte3_e32 v65, v121
	v_cvt_f32_ubyte2_e32 v64, v121
	v_pk_mul_f32 v[62:63], v[66:67], v[62:63]
	s_and_b64 vcc, exec, s[6:7]
	v_pk_mul_f32 v[64:65], v[68:69], v[64:65]
	s_cbranch_vccnz .LBB0_805
	v_lshlrev_b32_e32 v66, 16, v14
	v_and_b32_e32 v67, 0xffff0000, v14
	v_lshlrev_b32_e32 v14, 16, v15
	v_and_b32_e32 v15, 0xffff0000, v15
	v_pk_add_f32 v[60:61], v[60:61], v[14:15]
	v_lshlrev_b32_e32 v14, 16, v16
	v_and_b32_e32 v15, 0xffff0000, v16
	v_pk_add_f32 v[62:63], v[62:63], v[14:15]
	v_lshlrev_b32_e32 v14, 16, v17
	v_and_b32_e32 v15, 0xffff0000, v17
	v_pk_add_f32 v[58:59], v[58:59], v[66:67]
	v_pk_add_f32 v[64:65], v[64:65], v[14:15]

.LBB0_807:
	v_cvt_f32_i32_e32 v55, v55
	v_cvt_f32_i32_e32 v54, v54
	v_cvt_f32_i32_e32 v57, v57
	v_cvt_f32_i32_e32 v56, v56
	v_cvt_f32_i32_e32 v51, v51
	v_cvt_f32_i32_e32 v53, v53
	v_cvt_f32_i32_e32 v52, v52
	v_cvt_f32_i32_e32 v50, v50

	v_mul_f32_e32 v58, 0x36bae975, v142
	v_pk_mul_f32 v[56:57], v[58:59], v[56:57] op_sel_hi:[0,1]
	v_pk_mul_f32 v[54:55], v[58:59], v[54:55] op_sel_hi:[0,1]
	v_pk_mul_f32 v[60:61], v[58:59], v[52:53] op_sel_hi:[0,1]
	v_pk_mul_f32 v[58:59], v[58:59], v[50:51] op_sel_hi:[0,1]
	v_cvt_f32_ubyte1_e32 v51, v116
	v_cvt_f32_ubyte0_e32 v50, v116
	v_cvt_f32_ubyte3_e32 v53, v116
	v_cvt_f32_ubyte2_e32 v52, v116
	v_pk_mul_f32 v[50:51], v[54:55], v[50:51]
	v_pk_mul_f32 v[52:53], v[56:57], v[52:53]
	v_cvt_f32_ubyte1_e32 v55, v117
	v_cvt_f32_ubyte0_e32 v54, v117
	v_cvt_f32_ubyte3_e32 v57, v117
	v_cvt_f32_ubyte2_e32 v56, v117
	v_pk_mul_f32 v[54:55], v[58:59], v[54:55]
	s_and_b64 vcc, exec, s[6:7]
	v_pk_mul_f32 v[56:57], v[60:61], v[56:57]
	s_cbranch_vccnz .LBB0_809
	v_lshlrev_b32_e32 v58, 16, v10
	v_and_b32_e32 v59, 0xffff0000, v10
	v_lshlrev_b32_e32 v10, 16, v11
	v_and_b32_e32 v11, 0xffff0000, v11
	v_pk_add_f32 v[52:53], v[52:53], v[10:11]
	v_lshlrev_b32_e32 v10, 16, v12
	v_and_b32_e32 v11, 0xffff0000, v12
	v_pk_add_f32 v[54:55], v[54:55], v[10:11]
	v_lshlrev_b32_e32 v10, 16, v13
	v_and_b32_e32 v11, 0xffff0000, v13
	v_pk_add_f32 v[50:51], v[50:51], v[58:59]
	v_pk_add_f32 v[56:57], v[56:57], v[10:11]

.LBB0_811:
	v_cvt_f32_i32_e32 v47, v47
	v_cvt_f32_i32_e32 v46, v46
	v_cvt_f32_i32_e32 v49, v49
	v_cvt_f32_i32_e32 v48, v48
	v_cvt_f32_i32_e32 v43, v43
	v_cvt_f32_i32_e32 v45, v45
	v_cvt_f32_i32_e32 v44, v44
	v_cvt_f32_i32_e32 v42, v42

	v_mul_f32_e32 v50, 0x36bae975, v141
	v_pk_mul_f32 v[48:49], v[50:51], v[48:49] op_sel_hi:[0,1]
	v_pk_mul_f32 v[46:47], v[50:51], v[46:47] op_sel_hi:[0,1]
	v_pk_mul_f32 v[52:53], v[50:51], v[44:45] op_sel_hi:[0,1]
	v_pk_mul_f32 v[50:51], v[50:51], v[42:43] op_sel_hi:[0,1]
	v_cvt_f32_ubyte1_e32 v43, v112
	v_cvt_f32_ubyte0_e32 v42, v112
	v_cvt_f32_ubyte3_e32 v45, v112
	v_cvt_f32_ubyte2_e32 v44, v112
	v_pk_mul_f32 v[42:43], v[46:47], v[42:43]
	v_pk_mul_f32 v[44:45], v[48:49], v[44:45]
	v_cvt_f32_ubyte1_e32 v47, v113
	v_cvt_f32_ubyte0_e32 v46, v113
	v_cvt_f32_ubyte3_e32 v49, v113
	v_cvt_f32_ubyte2_e32 v48, v113
	v_pk_mul_f32 v[46:47], v[50:51], v[46:47]
	s_and_b64 vcc, exec, s[6:7]
	v_pk_mul_f32 v[48:49], v[52:53], v[48:49]
	s_cbranch_vccnz .LBB0_813
	v_lshlrev_b32_e32 v50, 16, v6
	v_and_b32_e32 v51, 0xffff0000, v6
	v_lshlrev_b32_e32 v6, 16, v7
	v_and_b32_e32 v7, 0xffff0000, v7
	v_pk_add_f32 v[44:45], v[44:45], v[6:7]
	v_lshlrev_b32_e32 v6, 16, v8
	v_and_b32_e32 v7, 0xffff0000, v8
	v_pk_add_f32 v[46:47], v[46:47], v[6:7]
	v_lshlrev_b32_e32 v6, 16, v9
	v_and_b32_e32 v7, 0xffff0000, v9
	v_pk_add_f32 v[42:43], v[42:43], v[50:51]
	v_pk_add_f32 v[48:49], v[48:49], v[6:7]

.LBB0_815:
	v_cvt_f32_i32_e32 v39, v39
	v_cvt_f32_i32_e32 v38, v38
	v_cvt_f32_i32_e32 v41, v41
	v_cvt_f32_i32_e32 v40, v40
	v_cvt_f32_i32_e32 v35, v35
	v_cvt_f32_i32_e32 v37, v37
	v_cvt_f32_i32_e32 v36, v36
	v_cvt_f32_i32_e32 v34, v34

	v_mul_f32_e32 v42, 0x36bae975, v140
	v_pk_mul_f32 v[40:41], v[42:43], v[40:41] op_sel_hi:[0,1]
	v_pk_mul_f32 v[38:39], v[42:43], v[38:39] op_sel_hi:[0,1]
	v_pk_mul_f32 v[44:45], v[42:43], v[36:37] op_sel_hi:[0,1]
	v_pk_mul_f32 v[42:43], v[42:43], v[34:35] op_sel_hi:[0,1]
	v_cvt_f32_ubyte1_e32 v35, v108
	v_cvt_f32_ubyte0_e32 v34, v108
	v_cvt_f32_ubyte3_e32 v37, v108
	v_cvt_f32_ubyte2_e32 v36, v108
	v_pk_mul_f32 v[34:35], v[38:39], v[34:35]
	v_pk_mul_f32 v[36:37], v[40:41], v[36:37]
	v_cvt_f32_ubyte1_e32 v39, v109
	v_cvt_f32_ubyte0_e32 v38, v109
	v_cvt_f32_ubyte3_e32 v41, v109
	v_cvt_f32_ubyte2_e32 v40, v109
	v_pk_mul_f32 v[38:39], v[42:43], v[38:39]
	s_and_b64 vcc, exec, s[6:7]
	v_pk_mul_f32 v[40:41], v[44:45], v[40:41]
	s_cbranch_vccnz .LBB0_817
	v_lshlrev_b32_e32 v42, 16, v2
	v_and_b32_e32 v43, 0xffff0000, v2
	v_lshlrev_b32_e32 v2, 16, v3
	v_and_b32_e32 v3, 0xffff0000, v3
	v_pk_add_f32 v[36:37], v[36:37], v[2:3]
	v_lshlrev_b32_e32 v2, 16, v4
	v_and_b32_e32 v3, 0xffff0000, v4
	v_pk_add_f32 v[38:39], v[38:39], v[2:3]
	v_lshlrev_b32_e32 v2, 16, v5
	v_and_b32_e32 v3, 0xffff0000, v5
	v_pk_add_f32 v[34:35], v[34:35], v[42:43]
	v_pk_add_f32 v[40:41], v[40:41], v[2:3]
